# LN2 row loop: the per-wave LDS copy of the next layer's vectors for the NEXT row is started right after the current row's last read of it (covered by the next row's mid-row wait) instead of copy-wait-
# speedup vs baseline: 1.0012x; 1.0012x over previous
; #define GAS __attribute__((address_space(1)))
; __device__ __forceinline__ unsigned pk2(float lo, float hi) { const f32x2 v = {lo, hi}; const bf16v2 b = __builtin_convertvector(v, bf16v2); return __builtin_bit_cast(unsigned, b); }
; __device__ __forceinline__ const float* mod_ptr(const Frame& F, int l, int row) { return (const float*)(F.ws + WS_MOD) + ((size_t)l * 17 + row_b(row)) * 6144; }
; __device__ __forceinline__ void ph_ln2(Frame& F, int l, int ntok, bool last) {
;     ...
;         const float* mdn = last ? md : mod_ptr(F, l + 1, row);
;         float xn[16];
; #pragma unroll
;         for (int j = 0; j < 4; ++j) { const f32x4 g = *(const GAS f32x4*)(lg + LN2_COL(j)), bb = *(const GAS f32x4*)(lb + LN2_COL(j));
; #pragma unroll
;             for (int e = 0; e < 4; ++e) xn[4 * j + e] = v[4 * j + e] * rstd * g[e] + bb[e]; }
;         if (last) { float* op = F.out + (size_t)row * DM;
; #pragma unroll
;             for (int j = 0; j < 4; ++j) *(GAS f32x4*)(op + LN2_COL(j)) = (f32x4){xn[4 * j], xn[4 * j + 1], xn[4 * j + 2], xn[4 * j + 3]}; }
;         else {
;             __builtin_nontemporal_store((u32x4){pk2(xn[0], xn[1]), pk2(xn[2], xn[3]), pk2(xn[4], xn[5]), pk2(xn[6], xn[7])}, (GAS u32x4*)(xr + cA)); __builtin_nontemporal_store((u32x4){pk2(xn[8], xn[9]), pk2(xn[10], xn[11]), pk2(xn[12], xn[13]), pk2(xn[14], xn[15])}, (GAS u32x4*)(xr + cA + 128));
;             bf16_t* xm = (bf16_t*)(F.ws + WS_XM) + (size_t)row * DM;
;             unsigned w[8];
; #pragma unroll
;             for (int j = 0; j < 4; ++j) { const f32x4 sh = *(const GAS f32x4*)(mdn + LN2_COL(j)), sc = *(const GAS f32x4*)(mdn + 1024 + LN2_COL(j));
;                 w[2 * j] = pk2(xn[4 * j] * (1.f + sc[0]) + sh[0], xn[4 * j + 1] * (1.f + sc[1]) + sh[1]); w[2 * j + 1] = pk2(xn[4 * j + 2] * (1.f + sc[2]) + sh[2], xn[4 * j + 3] * (1.f + sc[3]) + sh[3]); }
;             *(GAS u32x4*)(xm + cA) = (u32x4){w[0], w[1], w[2], w[3]}; *(GAS u32x4*)(xm + cA + 128) = (u32x4){w[4], w[5], w[6], w[7]};
.Lln2_nx_keep:
	ds_read_b128 v[68:71], v173
	ds_read_b128 v[28:31], v173 offset:1024
	ds_read_b128 v[72:75], v173 offset:2048
	s_nop 0
	ds_read_b128 v[76:79], v173 offset:3072
	s_waitcnt lgkmcnt(0)
	v_pk_add_f32 v[76:77], v[76:77], 1.0 op_sel_hi:[1,0]
	s_nop 0
	v_pk_fma_f32 v[28:29], v[16:17], v[76:77], v[28:29]
	v_pk_add_f32 v[76:77], v[78:79], 1.0 op_sel_hi:[1,0]
	v_cvt_pk_bf16_f32 v28, v28, v29
	v_pk_fma_f32 v[30:31], v[18:19], v[76:77], v[30:31]
	s_nop 0
	v_cvt_pk_bf16_f32 v29, v30, v31
	v_pk_add_f32 v[30:31], v[72:73], 1.0 op_sel_hi:[1,0]
	s_nop 0
	v_pk_fma_f32 v[30:31], v[12:13], v[30:31], v[68:69]
	v_pk_add_f32 v[68:69], v[74:75], 1.0 op_sel_hi:[1,0]
	v_cvt_pk_bf16_f32 v30, v30, v31
	v_pk_fma_f32 v[68:69], v[14:15], v[68:69], v[70:71]
	s_nop 0
	v_cvt_pk_bf16_f32 v31, v68, v69
	ds_read_b128 v[68:71], v173 offset:4096
	ds_read_b128 v[72:75], v173 offset:5120
	v_lshl_add_u64 v[80:81], v[38:39], 2, s[36:37]
	ds_read_b128 v[76:79], v173 offset:6144
	s_nop 0
	ds_read_b128 v[80:83], v173 offset:7168
	s_mov_b64 s[36:37], 0
	s_waitcnt lgkmcnt(0)
	s_min_i32 s86, s38, 0x10000
	s_ashr_i32 s86, s86, 12
	s_add_i32 s86, s86, s46
	s_mul_hi_u32 s87, s86, 0x6000
	s_mul_i32 s86, s86, 0x6000
	s_add_u32 s90, s47, s86
	s_addc_u32 s91, s48, s87
	s_cmp_eq_u32 s90, s88
	s_cbranch_scc1 .Lln2_nx_next_keep
	s_mov_b32 s88, s90
	s_add_u32 s86, s90, 0x1000
	s_addc_u32 s87, s91, 0
	s_lshl_b32 m0, s97, 13
	s_nop 0
	global_load_lds_dwordx4 v191, s[90:91]
	s_add_i32 m0, m0, 0x400
	s_nop 0
	global_load_lds_dwordx4 v40, s[90:91]
	s_add_i32 m0, m0, 0x400
	s_nop 0
	global_load_lds_dwordx4 v191, s[86:87]
	s_add_i32 m0, m0, 0x400
	s_nop 0
	global_load_lds_dwordx4 v40, s[86:87]
	s_add_i32 m0, m0, 0x400
	s_nop 0
	global_load_lds_dwordx4 v225, s[90:91]
	s_add_i32 m0, m0, 0x400
	s_nop 0
	global_load_lds_dwordx4 v224, s[90:91]
	s_add_i32 m0, m0, 0x400
	s_nop 0
	global_load_lds_dwordx4 v225, s[86:87]
	s_add_i32 m0, m0, 0x400
	s_nop 0
	global_load_lds_dwordx4 v224, s[86:87]
.Lln2_nx_next_keep:
	v_pk_add_f32 v[80:81], v[80:81], 1.0 op_sel_hi:[1,0]
	s_nop 0
	v_pk_fma_f32 v[72:73], v[24:25], v[80:81], v[72:73]
	v_pk_add_f32 v[80:81], v[82:83], 1.0 op_sel_hi:[1,0]
	v_cvt_pk_bf16_f32 v72, v72, v73
	v_pk_fma_f32 v[74:75], v[26:27], v[80:81], v[74:75]
	s_nop 0
	v_cvt_pk_bf16_f32 v73, v74, v75
	v_pk_add_f32 v[74:75], v[76:77], 1.0 op_sel_hi:[1,0]
	s_nop 0
	v_pk_fma_f32 v[68:69], v[20:21], v[74:75], v[68:69]
	s_nop 0
	v_cvt_pk_bf16_f32 v74, v68, v69
	v_pk_add_f32 v[68:69], v[78:79], 1.0 op_sel_hi:[1,0]
	s_nop 0
	v_pk_fma_f32 v[68:69], v[22:23], v[68:69], v[70:71]
	s_nop 0
	v_cvt_pk_bf16_f32 v75, v68, v69
	v_add_co_u32_e32 v68, vcc, 0x11b00000, v84
	s_nop 1
	v_addc_co_u32_e32 v69, vcc, 0, v85, vcc
	global_store_dwordx4 v[68:69], v[28:31], off
	global_store_dwordx4 v[68:69], v[72:75], off offset:256
